# v64 + softmax: fmaxf canonicalisation self-maxes and the '0 +' head of the row-sum chain removed
# baseline (speedup 1.0000x reference)
; DEV void partialSM(f32x16& p0, f32x16& p1, float& m_reg, float& mn, float& alpha) {
;   constexpr float C = SCALE * 1.4426950408889634f;
;   float pmax = p0[0];
; #pragma unroll
;   for (int r = 1; r < 16; ++r) pmax = fmaxf(pmax, p0[r]);
; #pragma unroll
;   for (int r = 0; r < 16; ++r) pmax = fmaxf(pmax, p1[r]);
;   { auto rr = __builtin_amdgcn_permlane32_swap(__float_as_uint(pmax), __float_as_uint(pmax), false, false);
;     pmax = fmaxf(__uint_as_float(rr[0]), __uint_as_float(rr[1])); }
;   if (__builtin_expect(__all(pmax - m_reg <= THR / SCALE), 1)) { mn = m_reg; alpha = 1.f; }
;   else { mn = fmaxf(m_reg, pmax); alpha = __builtin_amdgcn_exp2f((m_reg - mn) * C); m_reg = mn; }
.Lmv2_a:
	s_nop 8
	v_max_f32_e32 v66, v84, v85
	v_max3_f32 v66, v66, v86, v87
	v_max3_f32 v66, v66, v88, v89
	v_max3_f32 v66, v66, v90, v91
	v_max3_f32 v66, v66, v92, v93
	v_max3_f32 v66, v66, v94, v95
	v_max3_f32 v66, v66, v96, v97
	v_max3_f32 v66, v66, v98, v99
	v_max3_f32 v66, v66, v68, v69
	v_max3_f32 v66, v66, v70, v71
	v_max3_f32 v66, v66, v72, v73
	v_max3_f32 v66, v66, v74, v75
	v_max3_f32 v66, v66, v76, v77
	v_max3_f32 v66, v66, v78, v79
	v_max3_f32 v66, v66, v80, v81
	v_max3_f32 v66, v66, v82, v83
	v_mov_b32_e32 v219, v66
	s_nop 1
	v_permlane32_swap_b32_e32 v66, v219
	v_max_f32_e32 v66, v66, v219
	v_sub_f32_e32 v219, v66, v215
	v_cmp_ge_f32_e32 vcc, s31, v219
	s_cmp_eq_u64 vcc, exec
	s_cbranch_scc0 .Lresc_a
	v_mov_b32_e32 v219, 1.0
	s_branch .Lnor_a

; #define SBAR() __builtin_amdgcn_sched_barrier(0)
; #define PV_WAIT(n) do { asm volatile("s_waitcnt lgkmcnt(" #n ")" ::: "memory"); SBAR(); } while (0)
; DEV void partialSM(f32x16& p0, f32x16& p1, float& m_reg, float& mn, float& alpha) {
;     ...
;   const float mnC = -mn * C;
; #pragma unroll
;   for (int r = 0; r < 16; ++r) p0[r] = fmaf(p0[r], C, mnC);
; #pragma unroll
;   for (int r = 0; r < 16; ++r) p1[r] = fmaf(p1[r], C, mnC);
; #pragma unroll
;   for (int r = 0; r < 16; ++r) p0[r] = __builtin_amdgcn_exp2f(p0[r]);
; }
; DEV void finishSM(f32x16& p0, f32x16& p1, float alpha, float& l_reg, bf16x8& pa0, bf16x8& pa1, bf16x8& pa2, bf16x8& pa3) {
; #pragma unroll
;   for (int r = 0; r < 16; ++r) p1[r] = __builtin_amdgcn_exp2f(p1[r]);
;   float ps = 0;
; #pragma unroll
;   for (int r = 0; r < 16; ++r) ps += p0[r];
; #pragma unroll
;   for (int r = 0; r < 16; ++r) ps += p1[r];
;   { auto rr = __builtin_amdgcn_permlane32_swap(__float_as_uint(ps), __float_as_uint(ps), false, false);
;     ps = __uint_as_float(rr[0]) + __uint_as_float(rr[1]); }
;   l_reg = l_reg * alpha + ps;
;     ...
;   PK4(p0, 0, pa0); PK4(p0, 8, pa1); PK4(p1, 0, pa2); PK4(p1, 8, pa3);
;     ...
; }
; DEV void pv_mma(f32x16& od, const VFrag& f, bf16x8 pa0, bf16x8 pa1, bf16x8 pa2, bf16x8 pa3) {
;     ...
;   __builtin_amdgcn_s_setprio(1);
;   od = __builtin_amdgcn_mfma_f32_32x32x16_bf16(pa0, PK(f.l0, f.h0), od, 0, 0, 0);
;   od = __builtin_amdgcn_mfma_f32_32x32x16_bf16(pa1, PK(f.l1, f.h1), od, 0, 0, 0);
;   od = __builtin_amdgcn_mfma_f32_32x32x16_bf16(pa2, PK(f.l2, f.h2), od, 0, 0, 0);
;   od = __builtin_amdgcn_mfma_f32_32x32x16_bf16(pa3, PK(f.l3, f.h3), od, 0, 0, 0);
;   __builtin_amdgcn_s_setprio(0);
;     ...
; }
; DEV void pv_d0(f32x16* o, int vb, bf16x8 pa0, bf16x8 pa1, bf16x8 pa2, bf16x8 pa3) {
;   VFrag fa, fb;
;   pv_read<0>(fa, vb);
;   pv_read<1>(fb, vb); PV_WAIT(8); pv_mma(o[0], fa, pa0, pa1, pa2, pa3); SBAR();
;   pv_read<2>(fa, vb); PV_WAIT(8); pv_mma(o[1], fb, pa0, pa1, pa2, pa3); SBAR();
;   pv_read<3>(fb, vb); PV_WAIT(8); pv_mma(o[2], fa, pa0, pa1, pa2, pa3); SBAR();
;   PV_WAIT(0); pv_mma(o[3], fb, pa0, pa1, pa2, pa3);
.Lnor_a:
	v_mul_f32_e32 v66, 0xbdd53b94, v215
	v_fmamk_f32 v84, v84, 0x3dd53b94, v66
	v_fmamk_f32 v85, v85, 0x3dd53b94, v66
	v_fmamk_f32 v86, v86, 0x3dd53b94, v66
	v_fmamk_f32 v87, v87, 0x3dd53b94, v66
	v_fmamk_f32 v88, v88, 0x3dd53b94, v66
	v_fmamk_f32 v89, v89, 0x3dd53b94, v66
	v_fmamk_f32 v90, v90, 0x3dd53b94, v66
	v_fmamk_f32 v91, v91, 0x3dd53b94, v66
	v_fmamk_f32 v92, v92, 0x3dd53b94, v66
	v_fmamk_f32 v93, v93, 0x3dd53b94, v66
	v_fmamk_f32 v94, v94, 0x3dd53b94, v66
	v_fmamk_f32 v95, v95, 0x3dd53b94, v66
	v_fmamk_f32 v96, v96, 0x3dd53b94, v66
	v_fmamk_f32 v97, v97, 0x3dd53b94, v66
	v_fmamk_f32 v98, v98, 0x3dd53b94, v66
	v_fmamk_f32 v99, v99, 0x3dd53b94, v66
	v_fmamk_f32 v68, v68, 0x3dd53b94, v66
	v_fmamk_f32 v69, v69, 0x3dd53b94, v66
	v_fmamk_f32 v70, v70, 0x3dd53b94, v66
	v_fmamk_f32 v71, v71, 0x3dd53b94, v66
	v_fmamk_f32 v72, v72, 0x3dd53b94, v66
	v_fmamk_f32 v73, v73, 0x3dd53b94, v66
	v_fmamk_f32 v74, v74, 0x3dd53b94, v66
	v_fmamk_f32 v75, v75, 0x3dd53b94, v66
	v_fmamk_f32 v76, v76, 0x3dd53b94, v66
	v_fmamk_f32 v77, v77, 0x3dd53b94, v66
	v_fmamk_f32 v78, v78, 0x3dd53b94, v66
	v_fmamk_f32 v79, v79, 0x3dd53b94, v66
	v_fmamk_f32 v80, v80, 0x3dd53b94, v66
	v_fmamk_f32 v81, v81, 0x3dd53b94, v66
	v_fmamk_f32 v82, v82, 0x3dd53b94, v66
	v_fmac_f32_e32 v66, 0x3dd53b94, v83
	v_exp_f32_e32 v83, v84
	v_exp_f32_e32 v84, v85
	v_exp_f32_e32 v85, v86
	v_exp_f32_e32 v86, v87
	v_exp_f32_e32 v87, v88
	v_exp_f32_e32 v88, v89
	v_exp_f32_e32 v89, v90
	v_exp_f32_e32 v90, v91
	v_exp_f32_e32 v91, v92
	v_exp_f32_e32 v92, v93
	v_exp_f32_e32 v93, v94
	v_exp_f32_e32 v94, v95
	v_exp_f32_e32 v95, v96
	v_exp_f32_e32 v96, v97
	v_exp_f32_e32 v97, v98
	v_exp_f32_e32 v98, v99
	v_exp_f32_e32 v99, v68
	v_add_f32_e32 v68, v84, v83
	v_add_f32_e32 v68, v85, v68
	v_add_f32_e32 v68, v86, v68
	v_add_f32_e32 v68, v87, v68
	v_add_f32_e32 v68, v88, v68
	v_add_f32_e32 v68, v89, v68
	v_add_f32_e32 v68, v90, v68
	v_add_f32_e32 v68, v91, v68
	v_add_f32_e32 v68, v92, v68
	v_add_f32_e32 v68, v93, v68
	v_add_f32_e32 v68, v94, v68
	v_add_f32_e32 v68, v95, v68
	v_exp_f32_e32 v220, v69
	v_add_f32_e32 v68, v96, v68
	v_exp_f32_e32 v221, v70
	v_add_f32_e32 v68, v97, v68
	v_exp_f32_e32 v222, v71
	v_add_f32_e32 v68, v98, v68
	v_exp_f32_e32 v224, v72
	v_add_f32_e32 v68, v99, v68
	v_exp_f32_e32 v225, v73
	v_add_f32_e32 v68, v220, v68
	v_exp_f32_e32 v226, v74
	v_add_f32_e32 v68, v221, v68
	v_exp_f32_e32 v227, v75
	v_add_f32_e32 v68, v222, v68
	v_exp_f32_e32 v228, v76
	v_add_f32_e32 v68, v224, v68
	v_exp_f32_e32 v229, v77
	v_add_f32_e32 v68, v225, v68
	v_exp_f32_e32 v230, v78
	v_add_f32_e32 v68, v226, v68
	v_exp_f32_e32 v231, v79
	v_add_f32_e32 v68, v227, v68
	v_exp_f32_e32 v232, v80
	v_add_f32_e32 v68, v228, v68
	v_exp_f32_e32 v233, v81
	v_add_f32_e32 v68, v229, v68
	v_exp_f32_e32 v234, v82
	v_add_f32_e32 v68, v230, v68
	v_exp_f32_e32 v66, v66
	v_add_f32_e32 v68, v231, v68
	v_add_f32_e32 v68, v232, v68
	v_add_f32_e32 v68, v233, v68
	v_add_f32_e32 v68, v234, v68
	v_add_f32_e32 v68, v66, v68
	v_mov_b32_e32 v69, v68
	s_nop 1
	v_permlane32_swap_b32_e32 v68, v69
	v_cvt_pk_bf16_f32 v70, v83, v84
	v_cvt_pk_bf16_f32 v71, v85, v86
	v_cvt_pk_bf16_f32 v72, v87, v88
	v_cvt_pk_bf16_f32 v73, v89, v90
	v_cvt_pk_bf16_f32 v74, v91, v92
	v_cvt_pk_bf16_f32 v75, v93, v94
	v_cvt_pk_bf16_f32 v76, v95, v96
	v_cvt_pk_bf16_f32 v77, v97, v98
	v_cvt_pk_bf16_f32 v78, v99, v220
	v_cvt_pk_bf16_f32 v79, v221, v222
	v_cvt_pk_bf16_f32 v80, v224, v225
	v_cvt_pk_bf16_f32 v81, v226, v227
	v_cvt_pk_bf16_f32 v82, v228, v229
	v_cvt_pk_bf16_f32 v83, v230, v231
	v_cvt_pk_bf16_f32 v84, v232, v233
	v_cvt_pk_bf16_f32 v85, v234, v66
	v_permlane32_swap_b32_e32 v70, v72
	v_permlane32_swap_b32_e32 v71, v73
	v_permlane32_swap_b32_e32 v74, v76
	v_permlane32_swap_b32_e32 v75, v77
	v_permlane32_swap_b32_e32 v78, v80
	v_permlane32_swap_b32_e32 v79, v81
	v_permlane32_swap_b32_e32 v82, v84
	v_permlane32_swap_b32_e32 v83, v85
	v_lshl_add_u32 v66, s36, 14, v214
	ds_read_b64_tr_b16 v[86:87], v66 offset:0
	ds_read_b64_tr_b16 v[88:89], v66 offset:0x800
	ds_read_b64_tr_b16 v[90:91], v66 offset:0x1000
	ds_read_b64_tr_b16 v[92:93], v66 offset:0x1800
	ds_read_b64_tr_b16 v[94:95], v66 offset:0x2000
	ds_read_b64_tr_b16 v[96:97], v66 offset:0x2800
	ds_read_b64_tr_b16 v[224:225], v66 offset:0x3000
	ds_read_b64_tr_b16 v[226:227], v66 offset:0x3800
	ds_read_b64_tr_b16 v[228:229], v66 offset:0x200
	ds_read_b64_tr_b16 v[230:231], v66 offset:0xa00
	ds_read_b64_tr_b16 v[232:233], v66 offset:0x1200
	ds_read_b64_tr_b16 v[234:235], v66 offset:0x1a00
	ds_read_b64_tr_b16 v[236:237], v66 offset:0x2200
	ds_read_b64_tr_b16 v[238:239], v66 offset:0x2a00
	ds_read_b64_tr_b16 v[240:241], v66 offset:0x3200
	ds_read_b64_tr_b16 v[242:243], v66 offset:0x3a00
	s_waitcnt lgkmcnt(8)
	s_setprio 1
	v_mfma_f32_32x32x16_bf16 v[50:65], v[70:73], v[86:89], v[50:65]
	v_mfma_f32_32x32x16_bf16 v[50:65], v[74:77], v[90:93], v[50:65]
	v_mfma_f32_32x32x16_bf16 v[50:65], v[78:81], v[94:97], v[50:65]
	v_mfma_f32_32x32x16_bf16 v[50:65], v[82:85], v[224:227], v[50:65]
	s_setprio 0
	ds_read_b64_tr_b16 v[86:87], v66 offset:0x400
	ds_read_b64_tr_b16 v[88:89], v66 offset:0xc00
	ds_read_b64_tr_b16 v[90:91], v66 offset:0x1400
	ds_read_b64_tr_b16 v[92:93], v66 offset:0x1c00
	ds_read_b64_tr_b16 v[94:95], v66 offset:0x2400
	ds_read_b64_tr_b16 v[96:97], v66 offset:0x2c00
	ds_read_b64_tr_b16 v[224:225], v66 offset:0x3400
	ds_read_b64_tr_b16 v[226:227], v66 offset:0x3c00
	s_waitcnt lgkmcnt(8)
	s_setprio 1
	v_mfma_f32_32x32x16_bf16 v[34:49], v[70:73], v[228:231], v[34:49]
	v_mfma_f32_32x32x16_bf16 v[34:49], v[74:77], v[232:235], v[34:49]
	v_mfma_f32_32x32x16_bf16 v[34:49], v[78:81], v[236:239], v[34:49]
	v_mfma_f32_32x32x16_bf16 v[34:49], v[82:85], v[240:243], v[34:49]
	s_setprio 0
	ds_read_b64_tr_b16 v[228:229], v66 offset:0x600
	ds_read_b64_tr_b16 v[230:231], v66 offset:0xe00
	ds_read_b64_tr_b16 v[232:233], v66 offset:0x1600
	ds_read_b64_tr_b16 v[234:235], v66 offset:0x1e00
	ds_read_b64_tr_b16 v[236:237], v66 offset:0x2600
	ds_read_b64_tr_b16 v[238:239], v66 offset:0x2e00
	ds_read_b64_tr_b16 v[240:241], v66 offset:0x3600
	ds_read_b64_tr_b16 v[242:243], v66 offset:0x3e00
	s_waitcnt lgkmcnt(8)
	s_setprio 1
	v_mfma_f32_32x32x16_bf16 v[18:33], v[70:73], v[86:89], v[18:33]
	v_mfma_f32_32x32x16_bf16 v[18:33], v[74:77], v[90:93], v[18:33]
	v_mfma_f32_32x32x16_bf16 v[18:33], v[78:81], v[94:97], v[18:33]
	v_mfma_f32_32x32x16_bf16 v[18:33], v[82:85], v[224:227], v[18:33]
	s_setprio 0
	s_waitcnt lgkmcnt(0)
	s_setprio 1
	v_mfma_f32_32x32x16_bf16 v[2:17], v[70:73], v[228:231], v[2:17]
	v_mfma_f32_32x32x16_bf16 v[2:17], v[74:77], v[232:235], v[2:17]
	v_mfma_f32_32x32x16_bf16 v[2:17], v[78:81], v[236:239], v[2:17]
	v_mfma_f32_32x32x16_bf16 v[2:17], v[82:85], v[240:243], v[2:17]
	s_setprio 0
	s_cmp_gt_u32 s37, 62
	s_cbranch_scc1 .LBB0_919
; DEV int ltid() { int t = threadIdx.x; asm volatile("" : "+v"(t)); return t; }
; DEV unsigned cvt_pk4_fp8(f32x4 v) { unsigned r = 0; r = __builtin_amdgcn_cvt_pk_fp8_f32(v[0], v[1], r, false); r = __builtin_amdgcn_cvt_pk_fp8_f32(v[2], v[3], r, true); return r; }
; DEV void fill_load(CParams& p, int wg, int slot, f32x4 (&ld)[4]) {
;   const FillDesc d = fill_decode(p, wg, slot); const int tid = ltid(), tx = tid & 15, ty = tid >> 4;
;   const float* sp = d.src + (long)(d.kh + 4 * ty) * d.ldsrc + d.n0 + 4 * tx;
; #pragma unroll
;   for (int r = 0; r < 4; ++r) ld[r] = *(const f32x4*)(sp + (long)r * d.ldsrc);
; }
; DEV void fill_write(const f32x4 (&ld)[4], int bufsel) {
;   extern __shared__ __attribute__((aligned(16))) char shm[];
;   unsigned* T = (unsigned*)(shm + FILL_LDS_OFF + bufsel * FILL_TB); const int tid = ltid(), tx = tid & 15, ty = tid >> 4;
;   constexpr float WS = (float)(1 << FP8_WSCALE_LOG2_);
; #pragma unroll
;   for (int j = 0; j < 4; ++j) T[(4 * tx + j) * 33 + ty] = cvt_pk4_fp8((f32x4){ld[0][j] * WS, ld[1][j] * WS, ld[2][j] * WS, ld[3][j] * WS});
; }
; DEV void attn_unit(const bf16_t* __restrict__ Qb, const bf16_t* __restrict__ Kh, const bf16_t* __restrict__ Vh, const float* __restrict__ rp, bf16_t* __restrict__ Ob, CParams& fp, int fwg, int fbase, int fn) {
;     ...
;     if (j < fn) { fill_write(fld, j & 1); if (j + 1 < fn) fill_load(fp, fwg, fbase + j + 1, fld); }
	s_waitcnt vmcnt(3)
	v_mul_f32_e32 v71, 0x42800000, v168
	s_waitcnt vmcnt(2)
	v_mul_f32_e32 v72, 0x42800000, v172
	v_cvt_pk_fp8_f32 v73, v71, v72
	s_waitcnt vmcnt(1)
	v_mul_f32_e32 v71, 0x42800000, v176
	s_waitcnt vmcnt(0)
	v_mul_f32_e32 v72, 0x42800000, v180
	v_cvt_pk_fp8_f32 v73, v71, v72 op_sel:[0,0,1]
	v_mul_f32_e32 v71, 0x42800000, v169
	v_mul_f32_e32 v72, 0x42800000, v173
	v_cvt_pk_fp8_f32 v74, v71, v72
	v_mul_f32_e32 v71, 0x42800000, v177
	v_mul_f32_e32 v72, 0x42800000, v181
	v_cvt_pk_fp8_f32 v74, v71, v72 op_sel:[0,0,1]
	v_mul_f32_e32 v71, 0x42800000, v170
	v_mul_f32_e32 v72, 0x42800000, v174
	v_cvt_pk_fp8_f32 v77, v71, v72
	v_mul_f32_e32 v71, 0x42800000, v171
	v_mul_f32_e32 v72, 0x42800000, v175
	v_cvt_pk_fp8_f32 v78, v71, v72
	v_mul_f32_e32 v75, 0x42800000, v178
	v_mul_f32_e32 v76, 0x42800000, v182
	v_mul_f32_e32 v71, 0x42800000, v179
	v_mul_f32_e32 v72, 0x42800000, v183
	v_cvt_pk_fp8_f32 v77, v75, v76 op_sel:[0,0,1]
	v_cvt_pk_fp8_f32 v78, v71, v72 op_sel:[0,0,1]
	s_mul_i32 s56, s36, 0x2200
	s_cmp_eq_u32 s34, 60
	v_add_u32_e32 v66, s56, v245
	ds_write2_b32 v66, v73, v74 offset1:33
	ds_write2_b32 v66, v77, v78 offset0:66 offset1:99
	s_cbranch_scc1 .LBB0_919
	s_cmp_lg_u32 s37, 60
	s_cbranch_scc1 .Lfld_a
	s_mov_b64 s[62:63], s[20:21]
	v_mov_b32_e32 v248, v252
	v_add_u32_e32 v249, 0x2000, v252
	v_add_u32_e32 v250, 0x4000, v252
	v_add_u32_e32 v251, 0x6000, v252

; DEV void partialSM(f32x16& p0, f32x16& p1, float& m_reg, float& mn, float& alpha) {
;   constexpr float C = SCALE * 1.4426950408889634f;
;   float pmax = p0[0];
; #pragma unroll
;   for (int r = 1; r < 16; ++r) pmax = fmaxf(pmax, p0[r]);
; #pragma unroll
;   for (int r = 0; r < 16; ++r) pmax = fmaxf(pmax, p1[r]);
;   { auto rr = __builtin_amdgcn_permlane32_swap(__float_as_uint(pmax), __float_as_uint(pmax), false, false);
;     pmax = fmaxf(__uint_as_float(rr[0]), __uint_as_float(rr[1])); }
;   if (__builtin_expect(__all(pmax - m_reg <= THR / SCALE), 1)) { mn = m_reg; alpha = 1.f; }
;   else { mn = fmaxf(m_reg, pmax); alpha = __builtin_amdgcn_exp2f((m_reg - mn) * C); m_reg = mn; }
.Lmv2_b:
	s_nop 8
	v_max_f32_e32 v66, v84, v85
	v_max3_f32 v66, v66, v86, v87
	v_max3_f32 v66, v66, v88, v89
	v_max3_f32 v66, v66, v90, v91
	v_max3_f32 v66, v66, v92, v93
	v_max3_f32 v66, v66, v94, v95
	v_max3_f32 v66, v66, v96, v97
	v_max3_f32 v66, v66, v98, v99
	v_max3_f32 v66, v66, v68, v69
	v_max3_f32 v66, v66, v70, v71
	v_max3_f32 v66, v66, v72, v73
	v_max3_f32 v66, v66, v74, v75
	v_max3_f32 v66, v66, v76, v77
	v_max3_f32 v66, v66, v78, v79
	v_max3_f32 v66, v66, v80, v81
	v_max3_f32 v66, v66, v82, v83
	v_mov_b32_e32 v219, v66
	s_nop 1
	v_permlane32_swap_b32_e32 v66, v219
	v_max_f32_e32 v66, v66, v219
	v_sub_f32_e32 v219, v66, v215
	v_cmp_ge_f32_e32 vcc, s34, v219
	s_cmp_eq_u64 vcc, exec
	s_cbranch_scc0 .Lresc_b
	v_mov_b32_e32 v219, 1.0
	s_branch .Lnor_b

; #define SBAR() __builtin_amdgcn_sched_barrier(0)
; #define PV_WAIT(n) do { asm volatile("s_waitcnt lgkmcnt(" #n ")" ::: "memory"); SBAR(); } while (0)
; DEV void partialSM(f32x16& p0, f32x16& p1, float& m_reg, float& mn, float& alpha) {
;     ...
;   const float mnC = -mn * C;
; #pragma unroll
;   for (int r = 0; r < 16; ++r) p0[r] = fmaf(p0[r], C, mnC);
; #pragma unroll
;   for (int r = 0; r < 16; ++r) p1[r] = fmaf(p1[r], C, mnC);
; #pragma unroll
;   for (int r = 0; r < 16; ++r) p0[r] = __builtin_amdgcn_exp2f(p0[r]);
; }
; DEV void finishSM(f32x16& p0, f32x16& p1, float alpha, float& l_reg, bf16x8& pa0, bf16x8& pa1, bf16x8& pa2, bf16x8& pa3) {
; #pragma unroll
;   for (int r = 0; r < 16; ++r) p1[r] = __builtin_amdgcn_exp2f(p1[r]);
;   float ps = 0;
; #pragma unroll
;   for (int r = 0; r < 16; ++r) ps += p0[r];
; #pragma unroll
;   for (int r = 0; r < 16; ++r) ps += p1[r];
;   { auto rr = __builtin_amdgcn_permlane32_swap(__float_as_uint(ps), __float_as_uint(ps), false, false);
;     ps = __uint_as_float(rr[0]) + __uint_as_float(rr[1]); }
;   l_reg = l_reg * alpha + ps;
;     ...
;   PK4(p0, 0, pa0); PK4(p0, 8, pa1); PK4(p1, 0, pa2); PK4(p1, 8, pa3);
;     ...
; }
; DEV void pv_mma(f32x16& od, const VFrag& f, bf16x8 pa0, bf16x8 pa1, bf16x8 pa2, bf16x8 pa3) {
;     ...
;   __builtin_amdgcn_s_setprio(1);
;   od = __builtin_amdgcn_mfma_f32_32x32x16_bf16(pa0, PK(f.l0, f.h0), od, 0, 0, 0);
;   od = __builtin_amdgcn_mfma_f32_32x32x16_bf16(pa1, PK(f.l1, f.h1), od, 0, 0, 0);
;   od = __builtin_amdgcn_mfma_f32_32x32x16_bf16(pa2, PK(f.l2, f.h2), od, 0, 0, 0);
;   od = __builtin_amdgcn_mfma_f32_32x32x16_bf16(pa3, PK(f.l3, f.h3), od, 0, 0, 0);
;   __builtin_amdgcn_s_setprio(0);
;     ...
; }
; DEV void pv_d0(f32x16* o, int vb, bf16x8 pa0, bf16x8 pa1, bf16x8 pa2, bf16x8 pa3) {
;   VFrag fa, fb;
;   pv_read<0>(fa, vb);
;   pv_read<1>(fb, vb); PV_WAIT(8); pv_mma(o[0], fa, pa0, pa1, pa2, pa3); SBAR();
;   pv_read<2>(fa, vb); PV_WAIT(8); pv_mma(o[1], fb, pa0, pa1, pa2, pa3); SBAR();
;   pv_read<3>(fb, vb); PV_WAIT(8); pv_mma(o[2], fa, pa0, pa1, pa2, pa3); SBAR();
;   PV_WAIT(0); pv_mma(o[3], fb, pa0, pa1, pa2, pa3);
.Lnor_b:
	v_mul_f32_e32 v66, 0xbdd53b94, v215
	v_fmamk_f32 v84, v84, 0x3dd53b94, v66
	v_fmamk_f32 v85, v85, 0x3dd53b94, v66
	v_fmamk_f32 v86, v86, 0x3dd53b94, v66
	v_fmamk_f32 v87, v87, 0x3dd53b94, v66
	v_fmamk_f32 v88, v88, 0x3dd53b94, v66
	v_fmamk_f32 v89, v89, 0x3dd53b94, v66
	v_fmamk_f32 v90, v90, 0x3dd53b94, v66
	v_fmamk_f32 v91, v91, 0x3dd53b94, v66
	v_fmamk_f32 v92, v92, 0x3dd53b94, v66
	v_fmamk_f32 v93, v93, 0x3dd53b94, v66
	v_fmamk_f32 v94, v94, 0x3dd53b94, v66
	v_fmamk_f32 v95, v95, 0x3dd53b94, v66
	v_fmamk_f32 v96, v96, 0x3dd53b94, v66
	v_fmamk_f32 v97, v97, 0x3dd53b94, v66
	v_fmamk_f32 v98, v98, 0x3dd53b94, v66
	v_fmamk_f32 v99, v99, 0x3dd53b94, v66
	v_fmamk_f32 v68, v68, 0x3dd53b94, v66
	v_fmamk_f32 v69, v69, 0x3dd53b94, v66
	v_fmamk_f32 v70, v70, 0x3dd53b94, v66
	v_fmamk_f32 v71, v71, 0x3dd53b94, v66
	v_fmamk_f32 v72, v72, 0x3dd53b94, v66
	v_fmamk_f32 v73, v73, 0x3dd53b94, v66
	v_fmamk_f32 v74, v74, 0x3dd53b94, v66
	v_fmamk_f32 v75, v75, 0x3dd53b94, v66
	v_fmamk_f32 v76, v76, 0x3dd53b94, v66
	v_fmamk_f32 v77, v77, 0x3dd53b94, v66
	v_fmamk_f32 v78, v78, 0x3dd53b94, v66
	v_fmamk_f32 v79, v79, 0x3dd53b94, v66
	v_fmamk_f32 v80, v80, 0x3dd53b94, v66
	v_fmamk_f32 v81, v81, 0x3dd53b94, v66
	v_fmamk_f32 v82, v82, 0x3dd53b94, v66
	v_fmac_f32_e32 v66, 0x3dd53b94, v83
	v_exp_f32_e32 v83, v84
	v_exp_f32_e32 v84, v85
	v_exp_f32_e32 v85, v86
	v_exp_f32_e32 v86, v87
	v_exp_f32_e32 v87, v88
	v_exp_f32_e32 v88, v89
	v_exp_f32_e32 v89, v90
	v_exp_f32_e32 v90, v91
	v_exp_f32_e32 v91, v92
	v_exp_f32_e32 v92, v93
	v_exp_f32_e32 v93, v94
	v_exp_f32_e32 v94, v95
	v_exp_f32_e32 v95, v96
	v_exp_f32_e32 v96, v97
	v_exp_f32_e32 v97, v98
	v_exp_f32_e32 v98, v99
	v_exp_f32_e32 v99, v68
	v_add_f32_e32 v68, v84, v83
	v_add_f32_e32 v68, v85, v68
	v_add_f32_e32 v68, v86, v68
	v_add_f32_e32 v68, v87, v68
	v_add_f32_e32 v68, v88, v68
	v_add_f32_e32 v68, v89, v68
	v_add_f32_e32 v68, v90, v68
	v_add_f32_e32 v68, v91, v68
	v_add_f32_e32 v68, v92, v68
	v_add_f32_e32 v68, v93, v68
	v_add_f32_e32 v68, v94, v68
	v_add_f32_e32 v68, v95, v68
	v_exp_f32_e32 v220, v69
	v_add_f32_e32 v68, v96, v68
	v_exp_f32_e32 v221, v70
	v_add_f32_e32 v68, v97, v68
	v_exp_f32_e32 v222, v71
	v_add_f32_e32 v68, v98, v68
	v_exp_f32_e32 v224, v72
	v_add_f32_e32 v68, v99, v68
	v_exp_f32_e32 v225, v73
	v_add_f32_e32 v68, v220, v68
	v_exp_f32_e32 v226, v74
	v_add_f32_e32 v68, v221, v68
	v_exp_f32_e32 v227, v75
	v_add_f32_e32 v68, v222, v68
	v_exp_f32_e32 v228, v76
	v_add_f32_e32 v68, v224, v68
	v_exp_f32_e32 v229, v77
	v_add_f32_e32 v68, v225, v68
	v_exp_f32_e32 v230, v78
	v_add_f32_e32 v68, v226, v68
	v_exp_f32_e32 v231, v79
	v_add_f32_e32 v68, v227, v68
	v_exp_f32_e32 v232, v80
	v_add_f32_e32 v68, v228, v68
	v_exp_f32_e32 v233, v81
	v_add_f32_e32 v68, v229, v68
	v_exp_f32_e32 v234, v82
	v_add_f32_e32 v68, v230, v68
	v_exp_f32_e32 v66, v66
	v_add_f32_e32 v68, v231, v68
	v_add_f32_e32 v68, v232, v68
	v_add_f32_e32 v68, v233, v68
	v_add_f32_e32 v68, v234, v68
	v_add_f32_e32 v68, v66, v68
	v_mov_b32_e32 v69, v68
	s_nop 1
	v_permlane32_swap_b32_e32 v68, v69
	v_cvt_pk_bf16_f32 v70, v83, v84
	v_cvt_pk_bf16_f32 v71, v85, v86
	v_cvt_pk_bf16_f32 v72, v87, v88
	v_cvt_pk_bf16_f32 v73, v89, v90
	v_cvt_pk_bf16_f32 v74, v91, v92
	v_cvt_pk_bf16_f32 v75, v93, v94
	v_cvt_pk_bf16_f32 v76, v95, v96
	v_cvt_pk_bf16_f32 v77, v97, v98
	v_cvt_pk_bf16_f32 v78, v99, v220
	v_cvt_pk_bf16_f32 v79, v221, v222
	v_cvt_pk_bf16_f32 v80, v224, v225
	v_cvt_pk_bf16_f32 v81, v226, v227
	v_cvt_pk_bf16_f32 v82, v228, v229
	v_cvt_pk_bf16_f32 v83, v230, v231
	v_cvt_pk_bf16_f32 v84, v232, v233
	v_cvt_pk_bf16_f32 v85, v234, v66
	v_permlane32_swap_b32_e32 v70, v72
	v_permlane32_swap_b32_e32 v71, v73
	v_permlane32_swap_b32_e32 v74, v76
	v_permlane32_swap_b32_e32 v75, v77
	v_permlane32_swap_b32_e32 v78, v80
	v_permlane32_swap_b32_e32 v79, v81
	v_permlane32_swap_b32_e32 v82, v84
	v_permlane32_swap_b32_e32 v83, v85
	v_lshl_add_u32 v66, s37, 14, v214
	ds_read_b64_tr_b16 v[86:87], v66 offset:0
	ds_read_b64_tr_b16 v[88:89], v66 offset:0x800
	ds_read_b64_tr_b16 v[90:91], v66 offset:0x1000
	ds_read_b64_tr_b16 v[92:93], v66 offset:0x1800
	ds_read_b64_tr_b16 v[94:95], v66 offset:0x2000
	ds_read_b64_tr_b16 v[96:97], v66 offset:0x2800
	ds_read_b64_tr_b16 v[224:225], v66 offset:0x3000
	ds_read_b64_tr_b16 v[226:227], v66 offset:0x3800
	ds_read_b64_tr_b16 v[228:229], v66 offset:0x200
	ds_read_b64_tr_b16 v[230:231], v66 offset:0xa00
	ds_read_b64_tr_b16 v[232:233], v66 offset:0x1200
	ds_read_b64_tr_b16 v[234:235], v66 offset:0x1a00
	ds_read_b64_tr_b16 v[236:237], v66 offset:0x2200
	ds_read_b64_tr_b16 v[238:239], v66 offset:0x2a00
	ds_read_b64_tr_b16 v[240:241], v66 offset:0x3200
	ds_read_b64_tr_b16 v[242:243], v66 offset:0x3a00
	s_waitcnt lgkmcnt(8)
	s_setprio 1
	v_mfma_f32_32x32x16_bf16 v[50:65], v[70:73], v[86:89], v[50:65]
	v_mfma_f32_32x32x16_bf16 v[50:65], v[74:77], v[90:93], v[50:65]
	v_mfma_f32_32x32x16_bf16 v[50:65], v[78:81], v[94:97], v[50:65]
	v_mfma_f32_32x32x16_bf16 v[50:65], v[82:85], v[224:227], v[50:65]
	s_setprio 0
	ds_read_b64_tr_b16 v[86:87], v66 offset:0x400
	ds_read_b64_tr_b16 v[88:89], v66 offset:0xc00
	ds_read_b64_tr_b16 v[90:91], v66 offset:0x1400
	ds_read_b64_tr_b16 v[92:93], v66 offset:0x1c00
	ds_read_b64_tr_b16 v[94:95], v66 offset:0x2400
	ds_read_b64_tr_b16 v[96:97], v66 offset:0x2c00
	ds_read_b64_tr_b16 v[224:225], v66 offset:0x3400
	ds_read_b64_tr_b16 v[226:227], v66 offset:0x3c00
	s_waitcnt lgkmcnt(8)
	s_setprio 1
	v_mfma_f32_32x32x16_bf16 v[34:49], v[70:73], v[228:231], v[34:49]
	v_mfma_f32_32x32x16_bf16 v[34:49], v[74:77], v[232:235], v[34:49]
	v_mfma_f32_32x32x16_bf16 v[34:49], v[78:81], v[236:239], v[34:49]
	v_mfma_f32_32x32x16_bf16 v[34:49], v[82:85], v[240:243], v[34:49]
	s_setprio 0
	ds_read_b64_tr_b16 v[228:229], v66 offset:0x600
	ds_read_b64_tr_b16 v[230:231], v66 offset:0xe00
	ds_read_b64_tr_b16 v[232:233], v66 offset:0x1600
	ds_read_b64_tr_b16 v[234:235], v66 offset:0x1e00
	ds_read_b64_tr_b16 v[236:237], v66 offset:0x2600
	ds_read_b64_tr_b16 v[238:239], v66 offset:0x2e00
	ds_read_b64_tr_b16 v[240:241], v66 offset:0x3600
	ds_read_b64_tr_b16 v[242:243], v66 offset:0x3e00
	s_waitcnt lgkmcnt(8)
	s_setprio 1
	v_mfma_f32_32x32x16_bf16 v[18:33], v[70:73], v[86:89], v[18:33]
	v_mfma_f32_32x32x16_bf16 v[18:33], v[74:77], v[90:93], v[18:33]
	v_mfma_f32_32x32x16_bf16 v[18:33], v[78:81], v[94:97], v[18:33]
	v_mfma_f32_32x32x16_bf16 v[18:33], v[82:85], v[224:227], v[18:33]
	s_setprio 0
	s_waitcnt lgkmcnt(0)
	s_setprio 1
	v_mfma_f32_32x32x16_bf16 v[2:17], v[70:73], v[228:231], v[2:17]
	v_mfma_f32_32x32x16_bf16 v[2:17], v[74:77], v[232:235], v[2:17]
	v_mfma_f32_32x32x16_bf16 v[2:17], v[78:81], v[236:239], v[2:17]
	v_mfma_f32_32x32x16_bf16 v[2:17], v[82:85], v[240:243], v[2:17]
	s_setprio 0
	s_cmp_gt_u32 s38, 61
	s_cbranch_scc1 .LBB0_1126
; DEV int ltid() { int t = threadIdx.x; asm volatile("" : "+v"(t)); return t; }
; DEV unsigned cvt_pk4_fp8(f32x4 v) { unsigned r = 0; r = __builtin_amdgcn_cvt_pk_fp8_f32(v[0], v[1], r, false); r = __builtin_amdgcn_cvt_pk_fp8_f32(v[2], v[3], r, true); return r; }
; DEV void fill_load(CParams& p, int wg, int slot, f32x4 (&ld)[4]) {
;   const FillDesc d = fill_decode(p, wg, slot); const int tid = ltid(), tx = tid & 15, ty = tid >> 4;
;   const float* sp = d.src + (long)(d.kh + 4 * ty) * d.ldsrc + d.n0 + 4 * tx;
; #pragma unroll
;   for (int r = 0; r < 4; ++r) ld[r] = *(const f32x4*)(sp + (long)r * d.ldsrc);
; }
; DEV void fill_write(const f32x4 (&ld)[4], int bufsel) {
;   extern __shared__ __attribute__((aligned(16))) char shm[];
;   unsigned* T = (unsigned*)(shm + FILL_LDS_OFF + bufsel * FILL_TB); const int tid = ltid(), tx = tid & 15, ty = tid >> 4;
;   constexpr float WS = (float)(1 << FP8_WSCALE_LOG2_);
; #pragma unroll
;   for (int j = 0; j < 4; ++j) T[(4 * tx + j) * 33 + ty] = cvt_pk4_fp8((f32x4){ld[0][j] * WS, ld[1][j] * WS, ld[2][j] * WS, ld[3][j] * WS});
; }
; DEV void attn_unit(const bf16_t* __restrict__ Qb, const bf16_t* __restrict__ Kh, const bf16_t* __restrict__ Vh, const float* __restrict__ rp, bf16_t* __restrict__ Ob, CParams& fp, int fwg, int fbase, int fn) {
;     ...
;     if (j < fn) { fill_write(fld, j & 1); if (j + 1 < fn) fill_load(fp, fwg, fbase + j + 1, fld); }
	s_waitcnt vmcnt(3)
	v_mul_f32_e32 v71, 0x42800000, v168
	s_waitcnt vmcnt(2)
	v_mul_f32_e32 v72, 0x42800000, v172
	v_cvt_pk_fp8_f32 v73, v71, v72
	s_waitcnt vmcnt(1)
	v_mul_f32_e32 v71, 0x42800000, v176
	s_waitcnt vmcnt(0)
	v_mul_f32_e32 v72, 0x42800000, v180
	v_cvt_pk_fp8_f32 v73, v71, v72 op_sel:[0,0,1]
	v_mul_f32_e32 v71, 0x42800000, v169
	v_mul_f32_e32 v72, 0x42800000, v173
	v_cvt_pk_fp8_f32 v74, v71, v72
	v_mul_f32_e32 v71, 0x42800000, v177
	v_mul_f32_e32 v72, 0x42800000, v181
	v_cvt_pk_fp8_f32 v74, v71, v72 op_sel:[0,0,1]
	v_mul_f32_e32 v71, 0x42800000, v170
	v_mul_f32_e32 v72, 0x42800000, v174
	v_cvt_pk_fp8_f32 v77, v71, v72
	v_mul_f32_e32 v71, 0x42800000, v171
	v_mul_f32_e32 v72, 0x42800000, v175
	v_cvt_pk_fp8_f32 v78, v71, v72
	v_mul_f32_e32 v75, 0x42800000, v178
	v_mul_f32_e32 v76, 0x42800000, v182
	v_mul_f32_e32 v71, 0x42800000, v179
	v_mul_f32_e32 v72, 0x42800000, v183
	v_cvt_pk_fp8_f32 v77, v75, v76 op_sel:[0,0,1]
	v_cvt_pk_fp8_f32 v78, v71, v72 op_sel:[0,0,1]
	s_mul_i32 s56, s37, 0x2200
	s_cmp_eq_u32 s35, 59
	v_add_u32_e32 v66, s56, v245
	ds_write2_b32 v66, v73, v74 offset1:33
	ds_write2_b32 v66, v77, v78 offset0:66 offset1:99
	s_cbranch_scc1 .LBB0_1126
	global_load_dwordx4 v[168:171], v248, s[62:63]
	global_load_dwordx4 v[172:175], v249, s[62:63]
	global_load_dwordx4 v[176:179], v250, s[62:63]
	global_load_dwordx4 v[180:183], v251, s[62:63]
	s_add_u32 s62, s62, 0x800000
	s_addc_u32 s63, s63, 0
